# speedup vs baseline: 1.0968x; 1.0058x over previous
.Lw2k_tail:
	s_cmp_eq_u32 s96, 0
	s_cbranch_scc1 .Lw2k_end
	s_mov_b32 s26, 0
	s_cmp_eq_u32 s96, 0
	s_cbranch_scc1 .Lw2k_tissued
	s_mov_b64 s[30:31], s[92:93]
	s_mov_b64 s[32:33], s[94:95]
	global_load_dwordx4 v[8:11], v216, s[30:31] nt
	global_load_dwordx4 v[12:15], v216, s[30:31] offset:1024 nt
	s_add_u32 s92, s92, 0x400000
	s_addc_u32 s93, s93, 0
	s_add_u32 s94, s94, 0x200000
	s_addc_u32 s95, s95, 0
	s_sub_u32 s96, s96, 1
	s_add_i32 s26, s26, 1
	s_cmp_eq_u32 s96, 0
	s_cbranch_scc1 .Lw2k_tissued
	s_mov_b64 s[34:35], s[92:93]
	s_mov_b64 s[36:37], s[94:95]
	global_load_dwordx4 v[16:19], v216, s[34:35] nt
	global_load_dwordx4 v[20:23], v216, s[34:35] offset:1024 nt
	s_add_u32 s92, s92, 0x400000
	s_addc_u32 s93, s93, 0
	s_add_u32 s94, s94, 0x200000
	s_addc_u32 s95, s95, 0
	s_sub_u32 s96, s96, 1
	s_add_i32 s26, s26, 1
	s_cmp_eq_u32 s96, 0
	s_cbranch_scc1 .Lw2k_tissued
	s_mov_b64 s[38:39], s[92:93]
	s_mov_b64 s[40:41], s[94:95]
	global_load_dwordx4 v[24:27], v216, s[38:39] nt
	global_load_dwordx4 v[28:31], v216, s[38:39] offset:1024 nt
	s_add_u32 s92, s92, 0x400000
	s_addc_u32 s93, s93, 0
	s_add_u32 s94, s94, 0x200000
	s_addc_u32 s95, s95, 0
	s_sub_u32 s96, s96, 1
	s_add_i32 s26, s26, 1
	s_cmp_eq_u32 s96, 0
	s_cbranch_scc1 .Lw2k_tissued
	s_mov_b64 s[42:43], s[92:93]
	s_mov_b64 s[44:45], s[94:95]
	global_load_dwordx4 v[32:35], v216, s[42:43] nt
	global_load_dwordx4 v[36:39], v216, s[42:43] offset:1024 nt
	s_add_u32 s92, s92, 0x400000
	s_addc_u32 s93, s93, 0
	s_add_u32 s94, s94, 0x200000
	s_addc_u32 s95, s95, 0
	s_sub_u32 s96, s96, 1
	s_add_i32 s26, s26, 1
	s_cmp_eq_u32 s96, 0
	s_cbranch_scc1 .Lw2k_tissued
	s_mov_b64 s[46:47], s[92:93]
	s_mov_b64 s[48:49], s[94:95]
	global_load_dwordx4 v[40:43], v216, s[46:47] nt
	global_load_dwordx4 v[44:47], v216, s[46:47] offset:1024 nt
	s_add_u32 s92, s92, 0x400000
	s_addc_u32 s93, s93, 0
	s_add_u32 s94, s94, 0x200000
	s_addc_u32 s95, s95, 0
	s_sub_u32 s96, s96, 1
	s_add_i32 s26, s26, 1
	s_cmp_eq_u32 s96, 0
	s_cbranch_scc1 .Lw2k_tissued
	s_mov_b64 s[50:51], s[92:93]
	s_mov_b64 s[52:53], s[94:95]
	global_load_dwordx4 v[48:51], v216, s[50:51] nt
	global_load_dwordx4 v[52:55], v216, s[50:51] offset:1024 nt
	s_add_u32 s92, s92, 0x400000
	s_addc_u32 s93, s93, 0
	s_add_u32 s94, s94, 0x200000
	s_addc_u32 s95, s95, 0
	s_sub_u32 s96, s96, 1
	s_add_i32 s26, s26, 1
	s_cmp_eq_u32 s96, 0
	s_cbranch_scc1 .Lw2k_tissued
	s_mov_b64 s[54:55], s[92:93]
	s_mov_b64 s[56:57], s[94:95]
	global_load_dwordx4 v[56:59], v216, s[54:55] nt
	global_load_dwordx4 v[60:63], v216, s[54:55] offset:1024 nt
	s_add_u32 s92, s92, 0x400000
	s_addc_u32 s93, s93, 0
	s_add_u32 s94, s94, 0x200000
	s_addc_u32 s95, s95, 0
	s_sub_u32 s96, s96, 1
	s_add_i32 s26, s26, 1
	s_cmp_eq_u32 s96, 0
	s_cbranch_scc1 .Lw2k_tissued
	s_mov_b64 s[58:59], s[92:93]
	s_mov_b64 s[60:61], s[94:95]
	global_load_dwordx4 v[64:67], v216, s[58:59] nt
	global_load_dwordx4 v[68:71], v216, s[58:59] offset:1024 nt
	s_add_u32 s92, s92, 0x400000
	s_addc_u32 s93, s93, 0
	s_add_u32 s94, s94, 0x200000
	s_addc_u32 s95, s95, 0
	s_sub_u32 s96, s96, 1
	s_add_i32 s26, s26, 1
.Lw2k_tissued:
	s_waitcnt vmcnt(0)
	s_cmp_le_u32 s26, 0
	s_cbranch_scc1 .Lw2k_tstored
	v_cvt_pk_f16_f32 v8, v8, v9
	v_cvt_pk_f16_f32 v9, v10, v11
	v_cvt_pk_f16_f32 v10, v12, v13
	v_cvt_pk_f16_f32 v11, v14, v15
	global_store_dwordx2 v217, v[8:9], s[32:33]
	global_store_dwordx2 v217, v[10:11], s[32:33] offset:512
	s_cmp_le_u32 s26, 1
	s_cbranch_scc1 .Lw2k_tstored
	v_cvt_pk_f16_f32 v16, v16, v17
	v_cvt_pk_f16_f32 v17, v18, v19
	v_cvt_pk_f16_f32 v18, v20, v21
	v_cvt_pk_f16_f32 v19, v22, v23
	global_store_dwordx2 v217, v[16:17], s[36:37]
	global_store_dwordx2 v217, v[18:19], s[36:37] offset:512
	s_cmp_le_u32 s26, 2
	s_cbranch_scc1 .Lw2k_tstored
	v_cvt_pk_f16_f32 v24, v24, v25
	v_cvt_pk_f16_f32 v25, v26, v27
	v_cvt_pk_f16_f32 v26, v28, v29
	v_cvt_pk_f16_f32 v27, v30, v31
	global_store_dwordx2 v217, v[24:25], s[40:41]
	global_store_dwordx2 v217, v[26:27], s[40:41] offset:512
	s_cmp_le_u32 s26, 3
	s_cbranch_scc1 .Lw2k_tstored
	v_cvt_pk_f16_f32 v32, v32, v33
	v_cvt_pk_f16_f32 v33, v34, v35
	v_cvt_pk_f16_f32 v34, v36, v37
	v_cvt_pk_f16_f32 v35, v38, v39
	global_store_dwordx2 v217, v[32:33], s[44:45]
	global_store_dwordx2 v217, v[34:35], s[44:45] offset:512
	s_cmp_le_u32 s26, 4
	s_cbranch_scc1 .Lw2k_tstored
	v_cvt_pk_f16_f32 v40, v40, v41
	v_cvt_pk_f16_f32 v41, v42, v43
	v_cvt_pk_f16_f32 v42, v44, v45
	v_cvt_pk_f16_f32 v43, v46, v47
	global_store_dwordx2 v217, v[40:41], s[48:49]
	global_store_dwordx2 v217, v[42:43], s[48:49] offset:512
	s_cmp_le_u32 s26, 5
	s_cbranch_scc1 .Lw2k_tstored
	v_cvt_pk_f16_f32 v48, v48, v49
	v_cvt_pk_f16_f32 v49, v50, v51
	v_cvt_pk_f16_f32 v50, v52, v53
	v_cvt_pk_f16_f32 v51, v54, v55
	global_store_dwordx2 v217, v[48:49], s[52:53]
	global_store_dwordx2 v217, v[50:51], s[52:53] offset:512
	s_cmp_le_u32 s26, 6
	s_cbranch_scc1 .Lw2k_tstored
	v_cvt_pk_f16_f32 v56, v56, v57
	v_cvt_pk_f16_f32 v57, v58, v59
	v_cvt_pk_f16_f32 v58, v60, v61
	v_cvt_pk_f16_f32 v59, v62, v63
	global_store_dwordx2 v217, v[56:57], s[56:57]
	global_store_dwordx2 v217, v[58:59], s[56:57] offset:512
	s_cmp_le_u32 s26, 7
	s_cbranch_scc1 .Lw2k_tstored
	v_cvt_pk_f16_f32 v64, v64, v65
	v_cvt_pk_f16_f32 v65, v66, v67
	v_cvt_pk_f16_f32 v66, v68, v69
	v_cvt_pk_f16_f32 v67, v70, v71
	global_store_dwordx2 v217, v[64:65], s[60:61]
	global_store_dwordx2 v217, v[66:67], s[60:61] offset:512
.Lw2k_tstored:
	s_branch .Lw2k_tail
